# nt (streaming) hint on every weight-conversion tile load, including the decode-path loads and the phase-0 conversion loop; single-tile-ahead pipeline kept
# baseline (speedup 1.0000x reference)
; #define LAS __attribute__((address_space(3)))
; __device__ __forceinline__ void tr_tile8(const float* __restrict__ src, int N, const float* __restrict__ ksc, float wscale, unsigned char* __restrict__ dst, int ldd, int k0, int n0, int drow0, LAS unsigned* tl, int tid) {
;     const int c4 = (tid & 15) * 4, kq = tid >> 4;
;     const float* s0 = src + (size_t)(k0 + 4 * kq) * N + n0 + c4;
;     f32x4 a = *(const f32x4*)s0, b = *(const f32x4*)(s0 + N), c = *(const f32x4*)(s0 + 2 * (size_t)N), d = *(const f32x4*)(s0 + 3 * (size_t)N);
;     float sa = wscale, sb = wscale, sc = wscale, sd = wscale;
;     if (ksc) { sa *= ksc[k0 + 4 * kq]; sb *= ksc[k0 + 4 * kq + 1]; sc *= ksc[k0 + 4 * kq + 2]; sd *= ksc[k0 + 4 * kq + 3]; }
; #pragma unroll
;     for (int j = 0; j < 4; ++j) tl[(c4 + j) * 33 + kq] = pk4_fp8(a[j] * sa, b[j] * sb, c[j] * sc, d[j] * sd);
;     __syncthreads();
;     const int n = tid >> 3, seg = tid & 7;
;     unsigned w[4];
; #pragma unroll
;     for (int q = 0; q < 4; ++q) w[q] = tl[n * 33 + seg * 4 + q];
;     *(u32x4*)(dst + (size_t)(drow0 + n) * ldd + k0 + seg * 16) = (u32x4){w[0], w[1], w[2], w[3]};
;     __syncthreads();
; }
; __device__ __forceinline__ void run_tjob(const TJob& jb, int t, LAS unsigned* tl, int tid) {
;     const int ntn = jb.N / 64, ntk = jb.K / 128, per = ntn * ntk;
;     const int bi = t / per, r = t % per, tk = r / ntn, tn = r % ntn;
;     const int n0 = tn * 64;
;     const int drow0 = jb.gu ? (256 * (n0 >> 7) + (jb.gu == 2 ? 128 : 0) + (n0 & 127)) : n0;
;     if (jb.f8) tr_tile8(jb.src + (size_t)bi * jb.sbs, jb.N, jb.ksc, W8_SCALE, (unsigned char*)jb.dst + (size_t)bi * jb.dbs, jb.ldd, tk * 128, n0, drow0, tl, tid);
;     else tr_tile(jb.src + (size_t)bi * jb.sbs, jb.N, jb.ksc, jb.dst + (size_t)bi * jb.dbs, jb.ldd, tk * 128, n0, drow0, tl, tid);
.LBB0_14:
	s_and_b64 s[28:29], s[58:59], exec
	s_cselect_b32 s24, s25, s24
	s_lshr_b32 s25, s23, 2
	v_cvt_f32_u32_e32 v7, s25
	s_sub_i32 s28, 0, s25
	s_sub_i32 s24, s15, s24
	s_abs_i32 s44, s24
	v_rcp_iflag_f32_e32 v7, v7
	s_lshr_b32 s33, s23, 6
	s_ashr_i32 s29, s24, 31
	v_cvt_f32_ubyte0_e32 v8, s33
	v_mul_f32_e32 v7, 0x4f7ffffe, v7
	v_cvt_u32_f32_e32 v7, v7
	v_rcp_iflag_f32_e32 v9, v8
	v_readfirstlane_b32 s45, v7
	s_mul_i32 s28, s28, s45
	s_mul_hi_u32 s28, s45, s28
	s_add_i32 s45, s45, s28
	s_mul_hi_u32 s28, s44, s45
	s_mul_i32 s45, s28, s25
	s_sub_i32 s44, s44, s45
	s_add_i32 s47, s28, 1
	s_sub_i32 s45, s44, s25
	s_cmp_ge_u32 s44, s25
	s_cselect_b32 s28, s47, s28
	s_cselect_b32 s44, s45, s44
	s_add_i32 s45, s28, 1
	s_cmp_ge_u32 s44, s25
	s_cselect_b32 s28, s45, s28
	s_xor_b32 s28, s28, s29
	s_sub_i32 s47, s28, s29
	s_mul_i32 s25, s47, s25
	s_sub_i32 s44, s24, s25
	s_sext_i32_i16 s28, s44
	v_cvt_f32_i32_e32 v7, s28
	s_ashr_i32 s28, s28, 30
	s_or_b32 s45, s28, 1
	s_load_dwordx2 s[24:25], s[56:57], 0x0
	v_mul_f32_e32 v9, v7, v9
	v_trunc_f32_e32 v9, v9
	v_fma_f32 v7, -v9, v8, v7
	v_cvt_i32_f32_e32 v9, v9
	v_cmp_ge_f32_e64 s[28:29], |v7|, v8
	s_and_b64 s[28:29], s[28:29], exec
	s_cselect_b32 s28, s45, 0
	v_readfirstlane_b32 s29, v9
	s_add_i32 s28, s29, s28
	s_sext_i32_i16 s29, s28
	s_mul_i32 s28, s28, s33
	s_sub_i32 s28, s44, s28
	s_sext_i32_i16 s33, s28
	s_lshl_b32 s28, s33, 6
	s_lshl_b32 s33, s33, 7
	s_and_b32 s33, s33, 0xffffff00
	s_and_b32 s44, s28, 64
	s_or_b32 s33, s33, s44
	s_and_b64 s[44:45], s[54:55], exec
	s_mul_hi_i32 s45, s46, s47
	s_mul_i32 s44, s46, s47
	s_cselect_b32 s33, s28, s33
	s_lshl_b64 s[44:45], s[44:45], 2
	s_waitcnt lgkmcnt(0)
	s_add_u32 s24, s24, s44
	s_addc_u32 s25, s25, s45
	s_mul_i32 s45, s52, s47
	s_lshl_b32 s46, s29, 7
	s_mul_hi_i32 s44, s52, s47
	s_add_u32 s48, s48, s45
	v_add_u32_e32 v7, s46, v1
	s_addc_u32 s49, s49, s44
	v_mad_i64_i32 v[8:9], s[44:45], v7, s23, 0
	v_lshl_add_u64 v[8:9], v[8:9], 2, s[24:25]
	s_ashr_i32 s29, s28, 31
	v_lshl_add_u64 v[8:9], s[28:29], 2, v[8:9]
	v_lshl_add_u64 v[12:13], v[8:9], 0, v[2:3]
	s_lshl_b32 s36, s23, 2
	v_lshl_add_u64 v[16:17], v[12:13], 0, s[36:37]
	global_load_dwordx4 v[8:11], v[12:13], off nt
	v_lshl_add_u64 v[20:21], v[16:17], 0, s[36:37]
	global_load_dwordx4 v[12:15], v[16:17], off nt
	v_add_u32_e32 v24, s33, v4
	global_load_dwordx4 v[16:19], v[20:21], off nt
	v_lshl_add_u64 v[20:21], v[20:21], 0, s[36:37]
	global_load_dwordx4 v[20:23], v[20:21], off nt
	v_ashrrev_i32_e32 v25, 31, v24
	v_lshlrev_b64 v[24:25], 11, v[24:25]
	s_ashr_i32 s47, s46, 31
	s_add_i32 s15, s15, s50
	s_cmpk_gt_i32 s15, 0x67f
	s_waitcnt vmcnt(3)
	v_mul_f32_e32 v7, 0x42800000, v8
	v_mul_f32_e32 v8, 0x42800000, v9
	v_mul_f32_e32 v9, 0x42800000, v10
	v_mul_f32_e32 v10, 0x42800000, v11
	s_waitcnt vmcnt(2)
	v_mul_f32_e32 v11, 0x42800000, v12
	v_mul_f32_e32 v12, 0x42800000, v13
	v_mul_f32_e32 v13, 0x42800000, v14
	v_mul_f32_e32 v14, 0x42800000, v15
	v_cvt_pk_fp8_f32 v7, v7, v11
	v_cvt_pk_fp8_f32 v8, v8, v12
	v_cvt_pk_fp8_f32 v9, v9, v13
	v_cvt_pk_fp8_f32 v10, v10, v14
	s_waitcnt vmcnt(1)
	v_mul_f32_e32 v15, 0x42800000, v16
	v_mul_f32_e32 v11, 0x42800000, v17
	s_waitcnt vmcnt(0)
	v_mul_f32_e32 v14, 0x42800000, v20
	v_mul_f32_e32 v16, 0x42800000, v21
	v_mul_f32_e32 v12, 0x42800000, v18
	v_mul_f32_e32 v13, 0x42800000, v19
	v_mul_f32_e32 v17, 0x42800000, v22
	v_mul_f32_e32 v18, 0x42800000, v23
	v_cvt_pk_fp8_f32 v7, v15, v14 op_sel:[0,0,1]
	v_cvt_pk_fp8_f32 v8, v11, v16 op_sel:[0,0,1]
	v_cvt_pk_fp8_f32 v9, v12, v17 op_sel:[0,0,1]
	v_cvt_pk_fp8_f32 v10, v13, v18 op_sel:[0,0,1]
	ds_write2_b32 v5, v7, v8 offset1:33
	ds_write2_b32 v5, v9, v10 offset0:66 offset1:99
	s_waitcnt lgkmcnt(0)
	s_barrier
	ds_read2_b32 v[8:9], v6 offset1:1
	ds_read2_b32 v[10:11], v6 offset0:2 offset1:3
	v_lshl_add_u64 v[12:13], s[48:49], 0, v[24:25]
	v_lshl_add_u64 v[12:13], v[12:13], 0, s[46:47]
	v_lshl_add_u64 v[12:13], v[12:13], 0, v[232:233]
	s_waitcnt lgkmcnt(0)
	global_store_dwordx4 v[12:13], v[8:11], off
	s_barrier
	s_cbranch_scc1 .LBB0_22

; #define LAS __attribute__((address_space(3)))
; __device__ __forceinline__ void tr_tile8(const float* __restrict__ src, int N, const float* __restrict__ ksc, float wscale, unsigned char* __restrict__ dst, int ldd, int k0, int n0, int drow0, LAS unsigned* tl, int tid) {
;     const int c4 = (tid & 15) * 4, kq = tid >> 4;
;     const float* s0 = src + (size_t)(k0 + 4 * kq) * N + n0 + c4;
;     f32x4 a = *(const f32x4*)s0, b = *(const f32x4*)(s0 + N), c = *(const f32x4*)(s0 + 2 * (size_t)N), d = *(const f32x4*)(s0 + 3 * (size_t)N);
; __device__ __forceinline__ void run_tjob(const TJob& jb, int t, LAS unsigned* tl, int tid) {
;     const int ntn = jb.N / 64, ntk = jb.K / 128, per = ntn * ntk;
;     const int bi = t / per, r = t % per, tk = r / ntn, tn = r % ntn;
;     const int n0 = tn * 64;
;     const int drow0 = jb.gu ? (256 * (n0 >> 7) + (jb.gu == 2 ? 128 : 0) + (n0 & 127)) : n0;
;     if (jb.f8) tr_tile8(jb.src + (size_t)bi * jb.sbs, jb.N, jb.ksc, W8_SCALE, (unsigned char*)jb.dst + (size_t)bi * jb.dbs, jb.ldd, tk * 128, n0, drow0, tl, tid);
;     else tr_tile(jb.src + (size_t)bi * jb.sbs, jb.N, jb.ksc, jb.dst + (size_t)bi * jb.dbs, jb.ldd, tk * 128, n0, drow0, tl, tid);
.LBB0_404:
	s_and_b64 s[48:49], s[60:61], exec
	s_cselect_b32 s33, s24, s25
	s_and_b64 s[24:25], s[58:59], exec
	s_cselect_b32 s23, s33, s23
	s_lshr_b32 s33, s36, 6
	s_lshr_b32 s24, s28, 7
	s_mul_i32 s24, s33, s24
	v_cvt_f32_u32_e32 v0, s24
	s_sub_i32 s49, 0, s24
	s_sub_i32 s25, s15, s23
	s_abs_i32 s48, s25
	v_rcp_iflag_f32_e32 v0, v0
	s_ashr_i32 s23, s25, 31
	s_load_dwordx2 s[40:41], s[40:41], 0x0
	v_mul_f32_e32 v0, 0x4f7ffffe, v0
	v_cvt_u32_f32_e32 v0, v0
	s_nop 0
	v_readfirstlane_b32 s58, v0
	s_mul_i32 s49, s49, s58
	s_mul_hi_u32 s49, s58, s49
	s_add_i32 s58, s58, s49
	s_mul_hi_u32 s49, s48, s58
	s_mul_i32 s58, s49, s24
	s_sub_i32 s48, s48, s58
	s_add_i32 s59, s49, 1
	s_sub_i32 s58, s48, s24
	s_cmp_ge_u32 s48, s24
	s_cselect_b32 s49, s59, s49
	s_cselect_b32 s48, s58, s48
	s_add_i32 s58, s49, 1
	s_cmp_ge_u32 s48, s24
	s_cselect_b32 s48, s58, s49
	s_xor_b32 s48, s48, s23
	s_sub_i32 s23, s48, s23
	v_cvt_f32_i32_e32 v0, s33
	s_mul_i32 s24, s23, s24
	s_sub_i32 s48, s25, s24
	s_sext_i32_i16 s24, s48
	v_cvt_f32_i32_e32 v1, s24
	v_rcp_iflag_f32_e32 v2, v0
	s_ashr_i32 s24, s24, 30
	s_or_b32 s49, s24, 1
	v_mul_f32_e32 v2, v1, v2
	v_trunc_f32_e32 v2, v2
	v_fma_f32 v1, -v2, v0, v1
	v_cvt_i32_f32_e32 v2, v2
	v_cmp_ge_f32_e64 s[24:25], |v1|, v0
	s_and_b64 s[24:25], s[24:25], exec
	s_cselect_b32 s24, s49, 0
	v_readfirstlane_b32 s25, v2
	s_add_i32 s24, s25, s24
	s_sext_i32_i16 s59, s24
	s_mul_i32 s24, s24, s33
	s_sub_i32 s24, s48, s24
	s_sext_i32_i16 s25, s24
	s_ashr_i32 s24, s23, 31
	s_mul_i32 s33, s86, s24
	s_mul_hi_u32 s48, s86, s23
	s_add_i32 s33, s48, s33
	s_mul_i32 s48, s87, s23
	s_add_i32 s49, s33, s48
	s_mul_i32 s48, s86, s23
	s_lshl_b32 s58, s25, 6
	s_lshl_b64 s[48:49], s[48:49], 2
	s_waitcnt lgkmcnt(0)
	s_add_u32 s48, s40, s48
	s_addc_u32 s49, s41, s49
	s_lshl_b32 s40, s59, 7
	v_add_u32_e32 v20, s40, v17
	v_mad_u64_u32 v[0:1], s[60:61], v20, s36, 0
	v_ashrrev_i32_e32 v21, 31, v20
	v_mov_b32_e32 v2, v1
	v_mad_u64_u32 v[2:3], s[60:61], v21, s36, v[2:3]
	v_mov_b32_e32 v1, v2
	v_lshl_add_u64 v[0:1], v[0:1], 2, s[48:49]
	s_ashr_i32 s59, s58, 31
	v_lshl_add_u64 v[0:1], s[58:59], 2, v[0:1]
	v_lshl_add_u64 v[0:1], v[0:1], 0, v[232:233]
	s_or_b32 s100, s86, s87
	s_cmp_lg_u32 s100, 0
	s_cselect_b32 s100, s25, -1
	v_mov_b64_e32 v[64:65], v[0:1]
	s_lshl_b64 s[48:49], s[36:37], 2
	v_lshl_add_u64 v[2:3], v[0:1], 0, s[48:49]
	global_load_dwordx4 v[8:11], v[0:1], off nt
	global_load_dwordx4 v[12:15], v[2:3], off nt
	v_lshl_add_u64 v[0:1], v[2:3], 0, s[48:49]
	v_lshl_add_u64 v[4:5], v[0:1], 0, s[48:49]
	global_load_dwordx4 v[0:3], v[0:1], off nt
	s_nop 0
	global_load_dwordx4 v[4:7], v[4:5], off nt
	s_cmp_eq_u64 s[8:9], 0
	s_cbranch_scc1 .LBB0_443
	v_lshl_add_u64 v[20:21], v[20:21], 2, s[8:9]
	global_load_dwordx4 v[28:31], v[20:21], off
	s_waitcnt vmcnt(0)
	v_pk_mul_f32 v[22:23], v[28:29], s[16:17] op_sel_hi:[1,0]
	v_pk_mul_f32 v[20:21], v[30:31], s[16:17] op_sel_hi:[1,0]

; #define LAS __attribute__((address_space(3)))
; __device__ __forceinline__ void tr_tile8(const float* __restrict__ src, int N, const float* __restrict__ ksc, float wscale, unsigned char* __restrict__ dst, int ldd, int k0, int n0, int drow0, LAS unsigned* tl, int tid) {
;     const int c4 = (tid & 15) * 4, kq = tid >> 4;
;     const float* s0 = src + (size_t)(k0 + 4 * kq) * N + n0 + c4;
;     f32x4 a = *(const f32x4*)s0, b = *(const f32x4*)(s0 + N), c = *(const f32x4*)(s0 + 2 * (size_t)N), d = *(const f32x4*)(s0 + 3 * (size_t)N);
; __device__ __forceinline__ void run_tjob(const TJob& jb, int t, LAS unsigned* tl, int tid) {
;     const int ntn = jb.N / 64, ntk = jb.K / 128, per = ntn * ntk;
;     const int bi = t / per, r = t % per, tk = r / ntn, tn = r % ntn;
;     const int n0 = tn * 64;
;     const int drow0 = jb.gu ? (256 * (n0 >> 7) + (jb.gu == 2 ? 128 : 0) + (n0 & 127)) : n0;
;     if (jb.f8) tr_tile8(jb.src + (size_t)bi * jb.sbs, jb.N, jb.ksc, W8_SCALE, (unsigned char*)jb.dst + (size_t)bi * jb.dbs, jb.ldd, tk * 128, n0, drow0, tl, tid);
;     else tr_tile(jb.src + (size_t)bi * jb.sbs, jb.N, jb.ksc, jb.dst + (size_t)bi * jb.dbs, jb.ldd, tk * 128, n0, drow0, tl, tid);
.LBB0_586:
	s_and_b64 s[48:49], s[60:61], exec
	s_cselect_b32 s33, s24, s25
	s_and_b64 s[24:25], s[58:59], exec
	s_cselect_b32 s23, s33, s23
	s_lshr_b32 s33, s36, 6
	s_lshr_b32 s24, s28, 7
	s_mul_i32 s24, s33, s24
	v_cvt_f32_u32_e32 v0, s24
	s_sub_i32 s49, 0, s24
	s_sub_i32 s25, s15, s23
	s_abs_i32 s48, s25
	v_rcp_iflag_f32_e32 v0, v0
	s_ashr_i32 s23, s25, 31
	v_mul_f32_e32 v0, 0x4f7ffffe, v0
	v_cvt_u32_f32_e32 v0, v0
	s_nop 0
	v_readfirstlane_b32 s58, v0
	s_mul_i32 s49, s49, s58
	s_mul_hi_u32 s49, s58, s49
	s_add_i32 s58, s58, s49
	s_mul_hi_u32 s49, s48, s58
	s_mul_i32 s58, s49, s24
	s_sub_i32 s48, s48, s58
	s_add_i32 s59, s49, 1
	s_sub_i32 s58, s48, s24
	s_cmp_ge_u32 s48, s24
	s_cselect_b32 s49, s59, s49
	s_cselect_b32 s48, s58, s48
	s_add_i32 s58, s49, 1
	s_cmp_ge_u32 s48, s24
	s_cselect_b32 s48, s58, s49
	s_xor_b32 s48, s48, s23
	s_sub_i32 s23, s48, s23
	v_cvt_f32_i32_e32 v0, s33
	s_mul_i32 s24, s23, s24
	s_sub_i32 s58, s25, s24
	s_sext_i32_i16 s24, s58
	v_cvt_f32_i32_e32 v1, s24
	v_rcp_iflag_f32_e32 v2, v0
	s_ashr_i32 s24, s24, 30
	s_or_b32 s59, s24, 1
	s_load_dwordx2 s[48:49], s[64:65], 0x0
	v_mul_f32_e32 v2, v1, v2
	v_trunc_f32_e32 v2, v2
	v_fma_f32 v1, -v2, v0, v1
	v_cvt_i32_f32_e32 v2, v2
	v_cmp_ge_f32_e64 s[24:25], |v1|, v0
	s_and_b64 s[24:25], s[24:25], exec
	s_cselect_b32 s24, s59, 0
	v_readfirstlane_b32 s25, v2
	s_add_i32 s24, s25, s24
	s_sext_i32_i16 s61, s24
	s_mul_i32 s24, s24, s33
	s_sub_i32 s24, s58, s24
	s_sext_i32_i16 s25, s24
	s_ashr_i32 s24, s23, 31
	s_mul_i32 s33, s66, s24
	s_mul_hi_u32 s58, s66, s23
	s_add_i32 s33, s58, s33
	s_mul_i32 s58, s67, s23
	s_add_i32 s59, s33, s58
	s_mul_i32 s58, s66, s23
	s_lshl_b32 s60, s25, 6
	s_lshl_b64 s[58:59], s[58:59], 2
	s_waitcnt lgkmcnt(0)
	s_add_u32 s48, s48, s58
	s_addc_u32 s49, s49, s59
	s_lshl_b32 s58, s61, 7
	v_add_u32_e32 v20, s58, v17
	v_mad_u64_u32 v[0:1], s[64:65], v20, s36, 0
	v_ashrrev_i32_e32 v21, 31, v20
	v_mov_b32_e32 v2, v1
	v_mad_u64_u32 v[2:3], s[64:65], v21, s36, v[2:3]
	v_mov_b32_e32 v1, v2
	v_lshl_add_u64 v[0:1], v[0:1], 2, s[48:49]
	s_ashr_i32 s61, s60, 31
	v_lshl_add_u64 v[0:1], s[60:61], 2, v[0:1]
	v_lshl_add_u64 v[0:1], v[0:1], 0, v[232:233]
	s_or_b32 s100, s66, s67
	s_cmp_lg_u32 s100, 0
	s_cselect_b32 s100, s25, -1
	v_mov_b64_e32 v[64:65], v[0:1]
	s_lshl_b64 s[48:49], s[36:37], 2
	v_lshl_add_u64 v[2:3], v[0:1], 0, s[48:49]
	global_load_dwordx4 v[8:11], v[0:1], off nt
	global_load_dwordx4 v[12:15], v[2:3], off nt
	v_lshl_add_u64 v[0:1], v[2:3], 0, s[48:49]
	v_lshl_add_u64 v[4:5], v[0:1], 0, s[48:49]
	global_load_dwordx4 v[0:3], v[0:1], off nt
	s_nop 0
	global_load_dwordx4 v[4:7], v[4:5], off nt
	s_cmp_eq_u64 s[8:9], 0
	s_cbranch_scc1 .LBB0_625
	v_lshl_add_u64 v[20:21], v[20:21], 2, s[8:9]
	global_load_dwordx4 v[28:31], v[20:21], off
	s_waitcnt vmcnt(0)
	v_pk_mul_f32 v[22:23], v[28:29], s[16:17] op_sel_hi:[1,0]
	v_pk_mul_f32 v[20:21], v[30:31], s[16:17] op_sel_hi:[1,0]
